# baseline (speedup 1.0000x reference)
.LBB2_54:
	v_lshlrev_b32_e32 v3, 2, v0
	v_and_b32_e32 v10, 31, v0
	v_lshrrev_b32_e32 v0, 8, v0
	v_or_b32_e32 v0, s33, v0
	s_movk_i32 s4, 0x880
	s_waitcnt lgkmcnt(0)
	v_mov_b64_e32 v[4:5], s[72:73]
	v_mad_u64_u32 v[4:5], s[0:1], v0, s4, v[4:5]
	v_and_b32_e32 v0, 0x3fc, v3
	v_cmp_lt_i32_e32 vcc, v180, v181
	v_lshlrev_b32_e32 v6, 1, v0
	v_mov_b32_e32 v7, 0
	v_cndmask_b32_e32 v0, v179, v180, vcc
	v_lshlrev_b32_e32 v0, 2, v0
	ds_bpermute_b32 v0, v0, v2
	v_lshl_add_u64 v[4:5], v[4:5], 0, v[6:7]
	s_movk_i32 s0, 0x1000
	s_waitcnt vmcnt(1)
	v_cvt_pk_f16_f32 v8, v134, v135
	v_cvt_pk_f16_f32 v9, v136, v137
	s_waitcnt lgkmcnt(0)
	v_add_f32_e32 v0, v2, v0
	v_div_scale_f32 v6, s[2:3], v0, v0, 1.0
	v_rcp_f32_e32 v11, v6
	v_add_co_u32_e32 v2, vcc, s0, v4
	global_store_dwordx2 v[4:5], v[8:9], off
	s_waitcnt vmcnt(1)
	v_cvt_pk_f16_f32 v8, v130, v131
	v_cvt_pk_f16_f32 v9, v132, v133
	v_addc_co_u32_e32 v3, vcc, 0, v5, vcc
	global_store_dwordx2 v[2:3], v[8:9], off offset:256
	v_fma_f32 v2, -v6, v11, 1.0
	v_fmac_f32_e32 v11, v2, v11
	v_div_scale_f32 v2, vcc, 1.0, v0, 1.0
	v_mul_f32_e32 v3, v2, v11
	v_fma_f32 v4, -v6, v3, v2
	v_fmac_f32_e32 v3, v4, v11
	v_fma_f32 v2, -v6, v3, v2
	v_div_fmas_f32 v2, v2, v11, v3
	s_movk_i32 s0, 0x1200
	v_div_fixup_f32 v0, v2, v0, 1.0
	v_mad_u32_u24 v14, v177, s0, 0
	v_mul_u32_u24_e32 v2, 0x90, v10
	v_lshlrev_b32_e32 v3, 3, v171
	v_add3_u32 v6, v14, v2, v3
	v_pk_mul_f32 v[2:3], v[0:1], v[98:99] op_sel_hi:[0,1]
	v_pk_mul_f32 v[4:5], v[0:1], v[100:101] op_sel_hi:[0,1]
	v_cvt_pk_f16_f32 v2, v2, v3
	v_cvt_pk_f16_f32 v3, v4, v5
	v_pk_mul_f32 v[4:5], v[0:1], v[66:67] op_sel_hi:[0,1]
	v_pk_mul_f32 v[8:9], v[0:1], v[68:69] op_sel_hi:[0,1]
	v_cvt_pk_f16_f32 v4, v4, v5
	v_cvt_pk_f16_f32 v5, v8, v9
	v_pk_mul_f32 v[8:9], v[0:1], v[102:103] op_sel_hi:[0,1]
	v_pk_mul_f32 v[10:11], v[0:1], v[104:105] op_sel_hi:[0,1]
	v_cvt_pk_f16_f32 v8, v8, v9
	v_cvt_pk_f16_f32 v9, v10, v11
	v_pk_mul_f32 v[10:11], v[0:1], v[70:71] op_sel_hi:[0,1]
	v_pk_mul_f32 v[12:13], v[0:1], v[72:73] op_sel_hi:[0,1]
	s_waitcnt vmcnt(0)
	s_barrier
	v_cvt_pk_f16_f32 v10, v10, v11
	v_cvt_pk_f16_f32 v11, v12, v13
	ds_write2_b64 v6, v[2:3], v[8:9] offset1:2
	ds_write2_b64 v6, v[4:5], v[10:11] offset0:8 offset1:10
	v_pk_mul_f32 v[2:3], v[0:1], v[106:107] op_sel_hi:[0,1]
	v_pk_mul_f32 v[4:5], v[0:1], v[108:109] op_sel_hi:[0,1]
	v_cvt_pk_f16_f32 v2, v2, v3
	v_cvt_pk_f16_f32 v3, v4, v5
	v_pk_mul_f32 v[4:5], v[0:1], v[74:75] op_sel_hi:[0,1]
	v_pk_mul_f32 v[8:9], v[0:1], v[76:77] op_sel_hi:[0,1]
	v_cvt_pk_f16_f32 v4, v4, v5
	v_cvt_pk_f16_f32 v5, v8, v9
	v_pk_mul_f32 v[8:9], v[0:1], v[110:111] op_sel_hi:[0,1]
	v_pk_mul_f32 v[10:11], v[0:1], v[112:113] op_sel_hi:[0,1]
	v_cvt_pk_f16_f32 v8, v8, v9
	v_cvt_pk_f16_f32 v9, v10, v11
	v_pk_mul_f32 v[10:11], v[0:1], v[78:79] op_sel_hi:[0,1]
	v_pk_mul_f32 v[12:13], v[0:1], v[80:81] op_sel_hi:[0,1]
	v_lshlrev_b32_e32 v0, 5, v176
	v_cvt_pk_f16_f32 v10, v10, v11
	v_cvt_pk_f16_f32 v11, v12, v13
	ds_write2_b64 v6, v[2:3], v[8:9] offset0:4 offset1:6
	ds_write2_b64 v6, v[4:5], v[10:11] offset0:12 offset1:14
	v_lshl_or_b32 v0, s68, 11, v0
	v_mov_b64_e32 v[2:3], s[70:71]
	s_lshl_b32 s0, s66, 7
	v_lshrrev_b32_e32 v8, 3, v1
	s_mov_b32 s1, 0
	v_mad_i64_i32 v[2:3], s[2:3], v0, s4, v[2:3]
	s_and_b32 s0, s0, 0x780
	v_and_b32_e32 v6, 0x70, v170
	v_mul_u32_u24_e32 v0, 0x90, v8
	s_waitcnt lgkmcnt(0)
	v_lshl_add_u64 v[2:3], v[2:3], 0, s[0:1]
	v_add3_u32 v12, v14, v6, v0
	v_lshl_add_u64 v[4:5], v[2:3], 0, v[6:7]
	ds_read_b128 v[0:3], v12
	v_mul_u32_u24_e32 v6, 0x440, v8
	v_lshlrev_b32_e32 v6, 1, v6
	v_lshl_add_u64 v[8:9], v[4:5], 0, v[6:7]
	ds_read_b128 v[4:7], v12 offset:1152
	s_movk_i32 s0, 0x4000
	s_waitcnt lgkmcnt(1)
	global_store_dwordx4 v[8:9], v[0:3], off sc0 sc1
	s_nop 1
	v_add_co_u32_e32 v0, vcc, s0, v8
	s_nop 1
	v_addc_co_u32_e32 v1, vcc, 0, v9, vcc
	s_waitcnt lgkmcnt(0)
	global_store_dwordx4 v[0:1], v[4:7], off offset:1024 sc0 sc1
	ds_read_b128 v[0:3], v12 offset:2304
	ds_read_b128 v[4:7], v12 offset:3456
	v_add_co_u32_e32 v10, vcc, 0x8000, v8
	s_nop 1
	v_addc_co_u32_e32 v11, vcc, 0, v9, vcc
	s_waitcnt lgkmcnt(1)
	global_store_dwordx4 v[10:11], v[0:3], off offset:2048 sc0 sc1
	s_nop 1
	v_add_co_u32_e32 v0, vcc, 0xc000, v8
	s_nop 1
	v_addc_co_u32_e32 v1, vcc, 0, v9, vcc
	s_waitcnt lgkmcnt(0)
	global_store_dwordx4 v[0:1], v[4:7], off offset:3072 sc0 sc1
	s_endpgm
